# speedup vs baseline: 1.0152x; 1.0152x over previous
.LBB1_8:
	s_or_b64 exec, exec, s[4:5]
	s_waitcnt vmcnt(1)
	v_mov_b32_e32 v184, 1
	v_lshl_add_u32 v180, v176, 2, v172
	v_lshl_add_u32 v181, v177, 2, v172
	v_lshl_add_u32 v182, v178, 2, v172
	v_lshl_add_u32 v183, v179, 2, v172
	s_waitcnt lgkmcnt(0)
	ds_add_u32 v180, v184
	ds_add_u32 v181, v184
	ds_add_u32 v182, v184
	ds_add_u32 v183, v184
	s_waitcnt lgkmcnt(0)
	ds_read_b32 v151, v173
	s_waitcnt lgkmcnt(0)
	v_cvt_f32_i32_e32 v185, v151
	ds_write_b32 v173, v185 offset:256
	v_add_u32_e32 v10, v172, v2
	s_waitcnt vmcnt(1) lgkmcnt(0)
	s_barrier
	s_nop 0
	ds_read_b128 v[18:21], v10 offset:256
	ds_read_b128 v[22:25], v10 offset:288
	ds_read_b128 v[82:85], v10 offset:320
	ds_read_b128 v[86:89], v10 offset:352
	ds_read_b128 v[74:77], v10 offset:384
	ds_read_b128 v[78:81], v10 offset:416
	ds_read_b128 v[2:5], v213 offset:32768
	ds_read_b128 v[6:9], v213 offset:0
	ds_read_b128 v[66:69], v10 offset:448
	ds_read_b128 v[70:73], v10 offset:480
	ds_read_b128 v[10:13], v213 offset:1024
	s_waitcnt lgkmcnt(3)
	v_pk_mul_f32 v[26:27], v[8:9], v[20:21]
	v_pk_mul_f32 v[28:29], v[6:7], v[18:19]
	ds_read_b128 v[14:17], v213 offset:8192
	s_waitcnt lgkmcnt(1)
	v_pk_mul_f32 v[12:13], v[12:13], v[24:25]
	v_pk_mul_f32 v[10:11], v[10:11], v[22:23]
	v_pk_fma_f32 v[30:31], v[8:9], v[20:21], v[12:13]
	v_pk_fma_f32 v[32:33], v[6:7], v[18:19], v[10:11]
	v_cvt_pk_bf16_f32 v9, v12, v13
	v_cvt_pk_bf16_f32 v7, v26, v27
	v_cvt_pk_bf16_f32 v8, v10, v11
	v_cvt_pk_bf16_f32 v6, v28, v29
	ds_read_b128 v[10:13], v213 offset:33792
	s_nop 0
	v_mfma_f32_32x32x16_bf16 v[34:49], v[2:5], v[6:9], 0
	ds_read_b128 v[6:9], v213 offset:9216
	s_waitcnt lgkmcnt(2)
	v_mul_f32_e32 v26, v16, v20
	v_mul_f32_e32 v27, v17, v21
	v_pk_mul_f32 v[50:51], v[14:15], v[18:19]
	s_mov_b32 s4, 0x3727c5ac
	s_waitcnt lgkmcnt(0)
	v_pk_mul_f32 v[8:9], v[8:9], v[24:25]
	v_pk_mul_f32 v[28:29], v[6:7], v[22:23]
	v_pk_fma_f32 v[90:91], v[16:17], v[20:21], v[8:9]
	v_pk_fma_f32 v[92:93], v[14:15], v[18:19], v[28:29]
	ds_read_b128 v[14:17], v213 offset:2048
	v_cvt_pk_bf16_f32 v9, v8, v9
	v_cvt_pk_bf16_f32 v7, v26, v27
	v_cvt_pk_bf16_f32 v8, v28, v29
	ds_read_b128 v[26:29], v213 offset:3072
	v_cvt_pk_bf16_f32 v6, v50, v51
	s_waitcnt lgkmcnt(1)
	v_pk_mul_f32 v[94:95], v[14:15], v[82:83]
	s_mov_b32 s0, 0x3c800000
	v_mfma_f32_32x32x16_bf16 v[50:65], v[2:5], v[6:9], 0
	v_mul_f32_e32 v2, v16, v84
	v_mul_f32_e32 v3, v17, v85
	s_waitcnt lgkmcnt(0)
	v_mul_f32_e32 v4, v28, v88
	v_mul_f32_e32 v5, v29, v89
	v_pk_mul_f32 v[6:7], v[26:27], v[86:87]
	v_pk_fma_f32 v[8:9], v[16:17], v[84:85], v[4:5]
	v_cvt_pk_bf16_f32 v3, v2, v3
	v_pk_fma_f32 v[14:15], v[14:15], v[82:83], v[6:7]
	v_pk_add_f32 v[26:27], v[8:9], v[30:31]
	v_cvt_pk_bf16_f32 v5, v4, v5
	v_cvt_pk_bf16_f32 v4, v6, v7
	ds_read_b128 v[6:9], v213 offset:10240
	v_pk_add_f32 v[28:29], v[14:15], v[32:33]
	ds_read_b128 v[14:17], v213 offset:11264
	v_cvt_pk_bf16_f32 v2, v94, v95
	s_waitcnt lgkmcnt(1)
	v_pk_mul_f32 v[30:31], v[6:7], v[82:83]
	v_mov_b64_e32 v[152:153], s[4:5]
	v_mfma_f32_32x32x16_bf16 v[34:49], v[10:13], v[2:5], v[34:49]
	v_mul_f32_e32 v2, v8, v84
	v_mul_f32_e32 v3, v9, v85
	s_waitcnt lgkmcnt(0)
	v_mul_f32_e32 v4, v16, v88
	v_mul_f32_e32 v5, v17, v89
	v_pk_mul_f32 v[14:15], v[14:15], v[86:87]
	v_pk_fma_f32 v[8:9], v[8:9], v[84:85], v[4:5]
	v_pk_fma_f32 v[6:7], v[6:7], v[82:83], v[14:15]
	v_cvt_pk_bf16_f32 v5, v4, v5
	v_cvt_pk_bf16_f32 v3, v2, v3
	v_cvt_pk_bf16_f32 v4, v14, v15
	v_pk_add_f32 v[32:33], v[8:9], v[90:91]
	v_pk_add_f32 v[90:91], v[6:7], v[92:93]
	ds_read_b128 v[6:9], v213 offset:34816
	ds_read_b128 v[14:17], v213 offset:4096
	v_cvt_pk_bf16_f32 v2, v30, v31
	s_mov_b32 s13, 0
	s_mov_b64 s[6:7], 0
	v_mfma_f32_32x32x16_bf16 v[50:65], v[10:13], v[2:5], v[50:65]
	ds_read_b128 v[2:5], v213 offset:5120
	ds_read_b128 v[10:13], v213 offset:12288
	s_waitcnt lgkmcnt(2)
	v_pk_mul_f32 v[30:31], v[16:17], v[76:77]
	v_pk_mul_f32 v[92:93], v[14:15], v[74:75]
	s_waitcnt lgkmcnt(1)
	v_pk_mul_f32 v[4:5], v[4:5], v[80:81]
	v_pk_mul_f32 v[94:95], v[2:3], v[78:79]
	v_pk_fma_f32 v[2:3], v[16:17], v[76:77], v[4:5]
	v_cvt_pk_bf16_f32 v5, v4, v5
	v_pk_add_f32 v[96:97], v[2:3], v[26:27]
	v_cvt_pk_bf16_f32 v3, v30, v31
	v_cvt_pk_bf16_f32 v4, v94, v95
	v_cvt_pk_bf16_f32 v2, v92, v93
	v_pk_fma_f32 v[14:15], v[14:15], v[74:75], v[94:95]
	s_waitcnt lgkmcnt(0)
	v_pk_mul_f32 v[30:31], v[10:11], v[74:75]
	v_mfma_f32_32x32x16_bf16 v[34:49], v[6:9], v[2:5], v[34:49]
	ds_read_b128 v[2:5], v213 offset:13312
	v_add_f32_e32 v98, v14, v28
	v_add_f32_e32 v99, v15, v29
	ds_read_b128 v[14:17], v213 offset:35840
	v_pk_mul_f32 v[26:27], v[12:13], v[76:77]
	s_waitcnt lgkmcnt(1)
	v_pk_mul_f32 v[4:5], v[4:5], v[80:81]
	v_pk_mul_f32 v[28:29], v[2:3], v[78:79]
	v_pk_fma_f32 v[2:3], v[12:13], v[76:77], v[4:5]
	v_pk_fma_f32 v[10:11], v[10:11], v[74:75], v[28:29]
	v_pk_add_f32 v[32:33], v[2:3], v[32:33]
	v_pk_add_f32 v[92:93], v[10:11], v[90:91]
	ds_read_b128 v[10:13], v213 offset:6144
	v_cvt_pk_bf16_f32 v5, v4, v5
	v_cvt_pk_bf16_f32 v3, v26, v27
	v_cvt_pk_bf16_f32 v4, v28, v29
	ds_read_b128 v[26:29], v213 offset:7168
	v_cvt_pk_bf16_f32 v2, v30, v31
	s_waitcnt lgkmcnt(1)
	v_pk_mul_f32 v[30:31], v[10:11], v[66:67]
	v_mfma_f32_32x32x16_bf16 v[50:65], v[6:9], v[2:5], v[50:65]
	v_mul_f32_e32 v2, v12, v68
	v_mul_f32_e32 v3, v13, v69
	s_waitcnt lgkmcnt(0)
	v_mul_f32_e32 v4, v28, v72
	v_mul_f32_e32 v5, v29, v73
	v_pk_mul_f32 v[6:7], v[26:27], v[70:71]
	v_pk_fma_f32 v[8:9], v[12:13], v[68:69], v[4:5]
	v_cvt_pk_bf16_f32 v3, v2, v3
	v_pk_fma_f32 v[10:11], v[10:11], v[66:67], v[6:7]
	v_pk_add_f32 v[94:95], v[8:9], v[96:97]
	v_cvt_pk_bf16_f32 v5, v4, v5
	v_cvt_pk_bf16_f32 v4, v6, v7
	ds_read_b128 v[6:9], v213 offset:14336
	v_pk_add_f32 v[96:97], v[10:11], v[98:99]
	ds_read_b128 v[10:13], v213 offset:15360
	v_cvt_pk_bf16_f32 v2, v30, v31
	s_waitcnt lgkmcnt(1)
	v_pk_mul_f32 v[30:31], v[6:7], v[66:67]
	v_mfma_f32_32x32x16_bf16 v[34:49], v[14:17], v[2:5], v[34:49]
	s_waitcnt lgkmcnt(0)
	v_mul_f32_e32 v10, v10, v70
	v_mul_f32_e32 v11, v11, v71
	v_mul_f32_e32 v2, v8, v68
	v_mul_f32_e32 v3, v9, v69
	v_pk_mul_f32 v[4:5], v[12:13], v[72:73]
	v_pk_fma_f32 v[6:7], v[6:7], v[66:67], v[10:11]
	v_pk_fma_f32 v[8:9], v[8:9], v[68:69], v[4:5]
	v_pk_add_f32 v[92:93], v[6:7], v[92:93]
	v_cvt_pk_bf16_f32 v3, v2, v3
	v_pk_add_f32 v[90:91], v[8:9], v[32:33]
	v_cvt_pk_bf16_f32 v5, v4, v5
	v_cvt_pk_bf16_f32 v4, v10, v11
	ds_read_b128 v[26:29], v213 offset:36864
	ds_read_b128 v[6:9], v213 offset:16384
	v_cvt_pk_bf16_f32 v2, v30, v31
	ds_read_b128 v[98:101], v213 offset:25600
	ds_read_b128 v[102:105], v213 offset:37888
	v_mfma_f32_32x32x16_bf16 v[50:65], v[14:17], v[2:5], v[50:65]
	ds_read_b128 v[2:5], v213 offset:17408
	ds_read_b128 v[30:33], v213 offset:24576
	s_waitcnt lgkmcnt(4)
	v_pk_mul_f32 v[12:13], v[6:7], v[18:19]
	v_pk_mul_f32 v[10:11], v[8:9], v[20:21]
	s_waitcnt lgkmcnt(1)
	v_pk_mul_f32 v[14:15], v[2:3], v[22:23]
	v_pk_mul_f32 v[22:23], v[98:99], v[22:23]
	v_pk_fma_f32 v[112:113], v[6:7], v[18:19], v[14:15]
	s_waitcnt lgkmcnt(0)
	v_pk_mul_f32 v[114:115], v[30:31], v[18:19]
	v_pk_fma_f32 v[118:119], v[30:31], v[18:19], v[22:23]
	v_pk_mul_f32 v[4:5], v[4:5], v[24:25]
	v_pk_mul_f32 v[106:107], v[32:33], v[20:21]
	v_pk_mul_f32 v[24:25], v[100:101], v[24:25]
	ds_read_b128 v[98:101], v213 offset:18432
	v_cvt_pk_bf16_f32 v19, v106, v107
	ds_read_b128 v[106:109], v213 offset:19456
	v_pk_fma_f32 v[110:111], v[8:9], v[20:21], v[4:5]
	v_cvt_pk_bf16_f32 v5, v4, v5
	v_cvt_pk_bf16_f32 v3, v10, v11
	v_cvt_pk_bf16_f32 v4, v14, v15
	s_waitcnt lgkmcnt(0)
	v_pk_mul_f32 v[106:107], v[106:107], v[86:87]
	v_cvt_pk_bf16_f32 v2, v12, v13
	v_pk_mul_f32 v[120:121], v[98:99], v[82:83]
	v_pk_mul_f32 v[108:109], v[108:109], v[88:89]
	v_pk_fma_f32 v[98:99], v[98:99], v[82:83], v[106:107]
	v_mfma_f32_32x32x16_bf16 v[2:17], v[26:29], v[2:5], 0
	v_cvt_pk_bf16_f32 v18, v114, v115
	v_mul_f32_e32 v114, v100, v84
	v_mul_f32_e32 v115, v101, v85
	v_fma_f32 v100, v100, v84, v108
	v_fma_f32 v101, v101, v85, v109
	v_pk_add_f32 v[124:125], v[98:99], v[112:113]
	v_pk_add_f32 v[122:123], v[100:101], v[110:111]
	v_cvt_pk_bf16_f32 v101, v108, v109
	v_cvt_pk_bf16_f32 v100, v106, v107
	ds_read_b128 v[106:109], v213 offset:26624
	v_pk_fma_f32 v[116:117], v[32:33], v[20:21], v[24:25]
	v_cvt_pk_bf16_f32 v21, v24, v25
	v_cvt_pk_bf16_f32 v20, v22, v23
	ds_read_b128 v[110:113], v213 offset:27648
	v_cvt_pk_bf16_f32 v99, v114, v115
	v_mfma_f32_32x32x16_bf16 v[18:33], v[26:29], v[18:21], 0
	v_cvt_pk_bf16_f32 v98, v120, v121
	s_waitcnt lgkmcnt(1)
	v_mul_f32_e32 v114, v106, v82
	v_mul_f32_e32 v115, v107, v83
	s_waitcnt lgkmcnt(0)
	v_pk_mul_f32 v[86:87], v[110:111], v[86:87]
	v_pk_mul_f32 v[88:89], v[112:113], v[88:89]
	v_pk_fma_f32 v[82:83], v[106:107], v[82:83], v[86:87]
	v_mfma_f32_32x32x16_bf16 v[2:17], v[102:105], v[98:101], v[2:17]
	v_mul_f32_e32 v98, v108, v84
	v_mul_f32_e32 v99, v109, v85
	v_fma_f32 v84, v108, v84, v88
	v_fma_f32 v85, v109, v85, v89
	v_add_f32_e32 v108, v82, v118
	v_add_f32_e32 v109, v83, v119
	v_cvt_pk_bf16_f32 v83, v98, v99
	v_pk_add_f32 v[106:107], v[84:85], v[116:117]
	v_cvt_pk_bf16_f32 v85, v88, v89
	v_cvt_pk_bf16_f32 v84, v86, v87
	ds_read_b128 v[86:89], v213 offset:38912
	ds_read_b128 v[98:101], v213 offset:20480
	v_cvt_pk_bf16_f32 v82, v114, v115
	s_waitcnt lgkmcnt(0)
	v_pk_mul_f32 v[110:111], v[100:101], v[76:77]
	v_mfma_f32_32x32x16_bf16 v[18:33], v[102:105], v[82:85], v[18:33]
	ds_read_b128 v[82:85], v213 offset:21504
	ds_read_b128 v[102:105], v213 offset:28672
	v_mul_f32_e32 v112, v98, v74
	v_mul_f32_e32 v113, v99, v75
	s_waitcnt lgkmcnt(1)
	v_pk_mul_f32 v[84:85], v[84:85], v[80:81]
	v_pk_mul_f32 v[114:115], v[82:83], v[78:79]
	v_pk_fma_f32 v[82:83], v[100:101], v[76:77], v[84:85]
	v_cvt_pk_bf16_f32 v85, v84, v85
	v_pk_add_f32 v[116:117], v[82:83], v[122:123]
	v_cvt_pk_bf16_f32 v83, v110, v111
	v_cvt_pk_bf16_f32 v84, v114, v115
	v_cvt_pk_bf16_f32 v82, v112, v113
	v_pk_fma_f32 v[98:99], v[98:99], v[74:75], v[114:115]
	s_waitcnt lgkmcnt(0)
	v_pk_mul_f32 v[112:113], v[102:103], v[74:75]
	v_mfma_f32_32x32x16_bf16 v[2:17], v[86:89], v[82:85], v[2:17]
	ds_read_b128 v[82:85], v213 offset:29696
	v_add_f32_e32 v118, v98, v124
	v_add_f32_e32 v119, v99, v125
	v_mul_f32_e32 v110, v104, v76
	v_mul_f32_e32 v111, v105, v77
	ds_read_b128 v[98:101], v213 offset:39936
	s_waitcnt lgkmcnt(1)
	v_pk_mul_f32 v[78:79], v[82:83], v[78:79]
	v_pk_mul_f32 v[80:81], v[84:85], v[80:81]
	v_pk_fma_f32 v[74:75], v[102:103], v[74:75], v[78:79]
	v_pk_fma_f32 v[76:77], v[104:105], v[76:77], v[80:81]
	v_pk_add_f32 v[104:105], v[74:75], v[108:109]
	v_pk_add_f32 v[102:103], v[76:77], v[106:107]
	v_cvt_pk_bf16_f32 v77, v80, v81
	v_cvt_pk_bf16_f32 v76, v78, v79
	ds_read_b128 v[78:81], v213 offset:22528
	ds_read_b128 v[82:85], v213 offset:23552
	v_cvt_pk_bf16_f32 v75, v110, v111
	v_cvt_pk_bf16_f32 v74, v112, v113
	s_waitcnt lgkmcnt(0)
	v_pk_mul_f32 v[82:83], v[82:83], v[70:71]
	v_mfma_f32_32x32x16_bf16 v[18:33], v[86:89], v[74:77], v[18:33]
	v_mul_f32_e32 v74, v80, v68
	v_mul_f32_e32 v75, v81, v69
	v_mul_f32_e32 v76, v84, v72
	v_mul_f32_e32 v77, v85, v73
	v_mul_f32_e32 v86, v78, v66
	v_mul_f32_e32 v87, v79, v67
	v_pk_fma_f32 v[80:81], v[80:81], v[68:69], v[76:77]
	v_pk_fma_f32 v[78:79], v[78:79], v[66:67], v[82:83]
	v_cvt_pk_bf16_f32 v75, v74, v75
	v_pk_add_f32 v[88:89], v[80:81], v[116:117]
	v_pk_add_f32 v[106:107], v[78:79], v[118:119]
	ds_read_b128 v[78:81], v213 offset:30720
	v_cvt_pk_bf16_f32 v77, v76, v77
	v_cvt_pk_bf16_f32 v76, v82, v83
	ds_read_b128 v[82:85], v213 offset:31744
	v_cvt_pk_bf16_f32 v74, v86, v87
	s_waitcnt lgkmcnt(0)
	v_pk_mul_f32 v[72:73], v[84:85], v[72:73]
	v_mfma_f32_32x32x16_bf16 v[2:17], v[98:101], v[74:77], v[2:17]
	v_mul_f32_e32 v74, v80, v68
	v_mul_f32_e32 v75, v81, v69
	v_fma_f32 v68, v80, v68, v72
	v_fma_f32 v69, v81, v69, v73
	v_mul_f32_e32 v70, v82, v70
	v_mul_f32_e32 v71, v83, v71
	v_pk_add_f32 v[84:85], v[68:69], v[102:103]
	v_cvt_pk_bf16_f32 v69, v72, v73
	v_pk_mov_b32 v[72:73], v[96:97], v[94:95] op_sel:[1,0]
	v_mov_b32_e32 v97, v95
	v_pk_add_f32 v[72:73], v[72:73], v[96:97]
	v_pk_mul_f32 v[76:77], v[78:79], v[66:67]
	v_pk_fma_f32 v[66:67], v[78:79], v[66:67], v[70:71]
	v_pk_add_f32 v[72:73], v[72:73], v[72:73] op_sel:[0,1] op_sel_hi:[1,0]
	v_pk_add_f32 v[86:87], v[66:67], v[104:105]
	v_mov_b32_e32 v66, v72
	s_nop 1
	v_permlane32_swap_b32_e32 v72, v66
	v_add_f32_e32 v66, v72, v66
	v_cvt_pk_bf16_f32 v67, v74, v75
	v_rcp_f32_e32 v74, v66
	v_cvt_pk_bf16_f32 v68, v70, v71
	v_cvt_pk_bf16_f32 v66, v76, v77
	v_pk_mul_f32 v[70:71], v[46:47], v[74:75] op_sel_hi:[1,0]
	s_nop 0
	v_mfma_f32_32x32x16_bf16 v[18:33], v[98:101], v[66:69], v[18:33]
	v_mul_f32_e32 v66, v42, v74
	v_mul_f32_e32 v67, v43, v74
	v_pk_mov_b32 v[42:43], v[92:93], v[90:91] op_sel:[1,0]
	v_mov_b32_e32 v93, v91
	v_pk_add_f32 v[42:43], v[42:43], v[92:93]
	v_pk_mul_f32 v[68:69], v[44:45], v[74:75] op_sel_hi:[1,0]
	v_pk_add_f32 v[42:43], v[42:43], v[42:43] op_sel:[0,1] op_sel_hi:[1,0]
	v_pk_mov_b32 v[44:45], v[106:107], v[88:89] op_sel:[1,0]
	v_mov_b32_e32 v43, v42
	s_nop 1
	v_permlane32_swap_b32_e32 v42, v43
	v_add_f32_e32 v42, v42, v43
	v_rcp_f32_e32 v42, v42
	v_mov_b32_e32 v107, v89
	v_pk_add_f32 v[44:45], v[44:45], v[106:107]
	v_pk_mul_f32 v[72:73], v[48:49], v[74:75] op_sel_hi:[1,0]
	v_pk_add_f32 v[44:45], v[44:45], v[44:45] op_sel:[0,1] op_sel_hi:[1,0]
	v_pk_mul_f32 v[36:37], v[36:37], v[74:75] op_sel_hi:[1,0]
	v_pk_mul_f32 v[38:39], v[38:39], v[74:75] op_sel_hi:[1,0]
	v_pk_mul_f32 v[40:41], v[40:41], v[74:75] op_sel_hi:[1,0]
	v_pk_mul_f32 v[34:35], v[34:35], v[74:75] op_sel_hi:[1,0]
	v_pk_mul_f32 v[74:75], v[58:59], v[42:43] op_sel_hi:[1,0]
	v_pk_mul_f32 v[78:79], v[60:61], v[42:43] op_sel_hi:[1,0]
	v_pk_mul_f32 v[80:81], v[62:63], v[42:43] op_sel_hi:[1,0]
	v_pk_mul_f32 v[82:83], v[64:65], v[42:43] op_sel_hi:[1,0]
	v_pk_mul_f32 v[92:93], v[52:53], v[42:43] op_sel_hi:[1,0]
	v_mov_b32_e32 v43, v44
	s_nop 1
	v_permlane32_swap_b32_e32 v44, v43
	v_add_f32_e32 v43, v44, v43
	v_rcp_f32_e32 v76, v43
	v_pk_mul_f32 v[96:97], v[54:55], v[42:43] op_sel_hi:[1,0]
	v_pk_mul_f32 v[94:95], v[56:57], v[42:43] op_sel_hi:[1,0]
	v_pk_mul_f32 v[98:99], v[50:51], v[42:43] op_sel_hi:[1,0]
	v_pk_mul_f32 v[100:101], v[4:5], v[76:77] op_sel_hi:[1,0]
	v_pk_mov_b32 v[4:5], v[86:87], v[84:85] op_sel:[1,0]
	v_mov_b32_e32 v87, v85
	v_pk_add_f32 v[4:5], v[4:5], v[86:87]
	v_pk_mul_f32 v[102:103], v[6:7], v[76:77] op_sel_hi:[1,0]
	v_pk_add_f32 v[104:105], v[4:5], v[4:5] op_sel:[0,1] op_sel_hi:[1,0]
	v_cvt_pk_bf16_f32 v7, v40, v41
	ds_read_b128 v[84:87], v150 offset:52224
	ds_read_b128 v[50:53], v150 offset:35840
	ds_read_b128 v[54:57], v150 offset:36864
	ds_read_b128 v[58:61], v150 offset:37888
	ds_read_b128 v[62:65], v150 offset:38912
	v_cvt_pk_bf16_f32 v6, v38, v39
	v_cvt_pk_bf16_f32 v5, v36, v37
	v_cvt_pk_bf16_f32 v4, v34, v35
	ds_read_b128 v[88:91], v150 offset:53248
	ds_read_b128 v[34:37], v150 offset:39936
	ds_read_b128 v[38:41], v150 offset:40960
	ds_read_b128 v[42:45], v150 offset:41984
	ds_read_b128 v[46:49], v150 offset:43008
	v_cvt_pk_bf16_f32 v95, v94, v95
	v_cvt_pk_bf16_f32 v94, v96, v97
	v_cvt_pk_bf16_f32 v93, v92, v93
	v_cvt_pk_bf16_f32 v92, v98, v99
	s_waitcnt lgkmcnt(5)
	v_mfma_f32_32x32x16_bf16 v[50:65], v[84:87], v[4:7], v[50:65]
	v_mul_f32_e32 v10, v10, v76
	v_mul_f32_e32 v11, v11, v76
	v_mul_f32_e32 v12, v12, v76
	v_mul_f32_e32 v13, v13, v76
	v_mul_f32_e32 v8, v8, v76
	v_mul_f32_e32 v9, v9, v76
	v_mov_b32_e32 v77, v104
	s_nop 1
	v_permlane32_swap_b32_e32 v104, v77
	v_cvt_pk_bf16_f32 v73, v72, v73
	s_waitcnt lgkmcnt(0)
	v_mfma_f32_32x32x16_bf16 v[34:49], v[84:87], v[92:95], v[34:49]
	v_cvt_pk_bf16_f32 v72, v70, v71
	v_cvt_pk_bf16_f32 v70, v66, v67
	v_add_f32_e32 v66, v104, v77
	v_cvt_pk_bf16_f32 v71, v68, v69
	v_rcp_f32_e32 v104, v66
	v_cvt_pk_bf16_f32 v69, v82, v83
	v_cvt_pk_bf16_f32 v68, v80, v81
	v_cvt_pk_bf16_f32 v67, v78, v79
	v_cvt_pk_bf16_f32 v66, v74, v75
	ds_read_b128 v[78:81], v150 offset:54272
	v_mfma_f32_32x32x16_bf16 v[50:65], v[88:91], v[70:73], v[50:65]
	v_mul_f32_e32 v2, v2, v76
	v_mul_f32_e32 v3, v3, v76
	v_mul_f32_e32 v20, v20, v104
	v_mul_f32_e32 v21, v21, v104
	v_cvt_pk_bf16_f32 v85, v8, v9
	v_cvt_pk_bf16_f32 v82, v2, v3
	v_pk_mul_f32 v[2:3], v[22:23], v[104:105] op_sel_hi:[1,0]
	v_pk_mul_f32 v[8:9], v[24:25], v[104:105] op_sel_hi:[1,0]
	v_pk_mul_f32 v[18:19], v[18:19], v[104:105] op_sel_hi:[1,0]
	v_mfma_f32_32x32x16_bf16 v[34:49], v[88:91], v[66:69], v[34:49]
	v_cvt_pk_bf16_f32 v84, v102, v103
	v_cvt_pk_bf16_f32 v83, v100, v101
	ds_read_b128 v[86:89], v150 offset:55296
	v_cvt_pk_bf16_f32 v99, v8, v9
	v_cvt_pk_bf16_f32 v98, v2, v3
	v_cvt_pk_bf16_f32 v97, v20, v21
	v_cvt_pk_bf16_f32 v96, v18, v19
	s_waitcnt lgkmcnt(1)
	v_mfma_f32_32x32x16_bf16 v[50:65], v[78:81], v[82:85], v[50:65]
	v_mul_f32_e32 v2, v14, v76
	v_mul_f32_e32 v3, v15, v76
	v_mul_f32_e32 v8, v16, v76
	v_mul_f32_e32 v9, v17, v76
	v_mul_f32_e32 v14, v26, v104
	v_mul_f32_e32 v15, v27, v104
	v_cvt_pk_bf16_f32 v77, v8, v9
	v_cvt_pk_bf16_f32 v76, v2, v3
	v_cvt_pk_bf16_f32 v74, v10, v11
	v_pk_mul_f32 v[2:3], v[28:29], v[104:105] op_sel_hi:[1,0]
	v_mfma_f32_32x32x16_bf16 v[34:49], v[78:81], v[96:99], v[34:49]
	v_mul_f32_e32 v8, v30, v104
	v_mul_f32_e32 v9, v31, v104
	v_mul_f32_e32 v10, v32, v104
	v_mul_f32_e32 v11, v33, v104
	v_cvt_pk_bf16_f32 v75, v12, v13
	v_cvt_pk_bf16_f32 v81, v10, v11
	v_cvt_pk_bf16_f32 v80, v8, v9
	v_cvt_pk_bf16_f32 v79, v2, v3
	v_cvt_pk_bf16_f32 v78, v14, v15
	s_waitcnt lgkmcnt(0)
	v_mfma_f32_32x32x16_bf16 v[50:65], v[86:89], v[74:77], v[50:65]
	v_mfma_f32_32x32x16_bf16 v[34:49], v[86:89], v[78:81], v[34:49]
	ds_read_b128 v[86:89], v150 offset:56320
	ds_read_b128 v[18:21], v150 offset:44032
	ds_read_b128 v[22:25], v150 offset:45056
	ds_read_b128 v[26:29], v150 offset:46080
	ds_read_b128 v[30:33], v150 offset:47104
	ds_read_b128 v[100:103], v150 offset:57344
	s_waitcnt lgkmcnt(1)
	v_mfma_f32_32x32x16_bf16 v[18:33], v[86:89], v[4:7], v[18:33]
	ds_read_b128 v[2:5], v150 offset:48128
	ds_read_b128 v[6:9], v150 offset:49152
	ds_read_b128 v[10:13], v150 offset:50176
	ds_read_b128 v[14:17], v150 offset:51200
	s_waitcnt lgkmcnt(0)
	v_mfma_f32_32x32x16_bf16 v[2:17], v[86:89], v[92:95], v[2:17]
	v_mfma_f32_32x32x16_bf16 v[18:33], v[100:103], v[70:73], v[18:33]
	v_mfma_f32_32x32x16_bf16 v[2:17], v[100:103], v[66:69], v[2:17]
	ds_read_b128 v[66:69], v150 offset:58368
	ds_read_b128 v[70:73], v150 offset:59392
	s_waitcnt lgkmcnt(1)
	v_mfma_f32_32x32x16_bf16 v[18:33], v[66:69], v[82:85], v[18:33]
	v_mfma_f32_32x32x16_bf16 v[2:17], v[66:69], v[96:99], v[2:17]
	s_waitcnt lgkmcnt(0)
	v_mfma_f32_32x32x16_bf16 v[18:33], v[70:73], v[74:77], v[18:33]
	v_mfma_f32_32x32x16_bf16 v[2:17], v[70:73], v[78:81], v[2:17]
	s_nop 10
	v_mul_f32_e32 v66, v22, v22
	v_mul_f32_e32 v67, v23, v23
	v_mul_f32_e32 v68, v30, v30
	v_mul_f32_e32 v69, v31, v31
	v_mul_f32_e32 v70, v24, v24
	v_mul_f32_e32 v71, v25, v25
	v_pk_mul_f32 v[72:73], v[32:33], v[32:33]
	v_pk_mul_f32 v[74:75], v[20:21], v[20:21]
	v_pk_mul_f32 v[76:77], v[28:29], v[28:29]
	v_pk_mul_f32 v[78:79], v[26:27], v[26:27]
	v_pk_mul_f32 v[80:81], v[18:19], v[18:19]
	v_pk_fma_f32 v[78:79], v[58:59], v[58:59], v[78:79]
	v_pk_fma_f32 v[76:77], v[60:61], v[60:61], v[76:77]
	v_pk_fma_f32 v[74:75], v[52:53], v[52:53], v[74:75]
	v_pk_fma_f32 v[72:73], v[64:65], v[64:65], v[72:73]
	v_pk_fma_f32 v[70:71], v[56:57], v[56:57], v[70:71]
	v_pk_fma_f32 v[68:69], v[62:63], v[62:63], v[68:69]
	v_pk_fma_f32 v[66:67], v[54:55], v[54:55], v[66:67]
	v_pk_fma_f32 v[80:81], v[50:51], v[50:51], v[80:81]
	v_pk_add_f32 v[66:67], v[66:67], v[68:69]
	v_pk_add_f32 v[68:69], v[70:71], v[72:73]
	v_pk_add_f32 v[70:71], v[74:75], v[76:77]
	v_pk_add_f32 v[72:73], v[80:81], v[78:79]
	v_pk_add_f32 v[68:69], v[70:71], v[68:69]
	v_pk_add_f32 v[66:67], v[72:73], v[66:67]
	v_pk_mul_f32 v[72:73], v[14:15], v[14:15]
	v_pk_mov_b32 v[70:71], v[66:67], v[68:69] op_sel:[1,0]
	v_mov_b32_e32 v67, v69
	v_pk_add_f32 v[66:67], v[70:71], v[66:67]
	v_pk_mul_f32 v[70:71], v[6:7], v[6:7]
	v_pk_mul_f32 v[74:75], v[8:9], v[8:9]
	v_pk_mul_f32 v[76:77], v[16:17], v[16:17]
	v_pk_mul_f32 v[78:79], v[4:5], v[4:5]
	v_pk_mul_f32 v[80:81], v[12:13], v[12:13]
	v_pk_mul_f32 v[82:83], v[10:11], v[10:11]
	v_pk_mul_f32 v[84:85], v[2:3], v[2:3]
	v_pk_fma_f32 v[82:83], v[42:43], v[42:43], v[82:83]
	v_pk_fma_f32 v[80:81], v[44:45], v[44:45], v[80:81]
	v_pk_fma_f32 v[78:79], v[36:37], v[36:37], v[78:79]
	v_pk_fma_f32 v[76:77], v[48:49], v[48:49], v[76:77]
	v_pk_fma_f32 v[74:75], v[40:41], v[40:41], v[74:75]
	v_pk_fma_f32 v[72:73], v[46:47], v[46:47], v[72:73]
	v_pk_fma_f32 v[70:71], v[38:39], v[38:39], v[70:71]
	v_pk_fma_f32 v[84:85], v[34:35], v[34:35], v[84:85]
	v_pk_add_f32 v[70:71], v[70:71], v[72:73]
	v_pk_add_f32 v[72:73], v[74:75], v[76:77]
	v_pk_add_f32 v[74:75], v[78:79], v[80:81]
	v_pk_add_f32 v[76:77], v[84:85], v[82:83]
	v_pk_add_f32 v[72:73], v[74:75], v[72:73]
	v_pk_add_f32 v[70:71], v[76:77], v[70:71]
	v_pk_add_f32 v[66:67], v[66:67], v[66:67] op_sel:[0,1] op_sel_hi:[1,0]
	v_pk_mov_b32 v[74:75], v[70:71], v[72:73] op_sel:[1,0]
	v_mov_b32_e32 v71, v73
	v_pk_add_f32 v[70:71], v[74:75], v[70:71]
	v_mov_b32_e32 v69, v66
	v_pk_add_f32 v[70:71], v[70:71], v[70:71] op_sel:[0,1] op_sel_hi:[1,0]
	s_nop 0
	v_permlane32_swap_b32_e32 v66, v69
	v_mov_b32_e32 v68, v70
	s_nop 1
	v_permlane32_swap_b32_e32 v70, v68
	v_mov_b32_e32 v71, v66
	v_pk_add_f32 v[66:67], v[70:71], v[68:69]
	v_pk_fma_f32 v[66:67], v[66:67], s[0:1], v[152:153] op_sel_hi:[1,0,0]
	s_mov_b32 s1, 0x800000
	v_mul_f32_e32 v68, 0x4b800000, v67
	v_cmp_gt_f32_e32 vcc, s1, v67
	s_nop 1
	v_cndmask_b32_e32 v67, v67, v68, vcc
	v_rsq_f32_e32 v67, v67
	s_nop 0
	v_mul_f32_e32 v68, 0x45800000, v67
	v_cndmask_b32_e32 v68, v67, v68, vcc
	v_pk_mul_f32 v[158:159], v[50:51], v[68:69] op_sel_hi:[1,0]
	v_pk_mul_f32 v[50:51], v[18:19], v[68:69] op_sel_hi:[1,0]
	v_mul_f32_e32 v18, 0x4b800000, v66
	v_cmp_gt_f32_e32 vcc, s1, v66
	v_pk_mul_f32 v[80:81], v[60:61], v[68:69] op_sel_hi:[1,0]
	v_pk_mul_f32 v[60:61], v[28:29], v[68:69] op_sel_hi:[1,0]
	v_cndmask_b32_e32 v18, v66, v18, vcc
	v_rsq_f32_e32 v18, v18
	v_pk_mul_f32 v[78:79], v[58:59], v[68:69] op_sel_hi:[1,0]
	v_pk_mul_f32 v[160:161], v[52:53], v[68:69] op_sel_hi:[1,0]
	v_pk_mul_f32 v[82:83], v[54:55], v[68:69] op_sel_hi:[1,0]
	v_mul_f32_e32 v19, 0x45800000, v18
	v_cndmask_b32_e32 v28, v18, v19, vcc
	v_pk_mul_f32 v[168:169], v[56:57], v[68:69] op_sel_hi:[1,0]
	v_pk_mul_f32 v[58:59], v[26:27], v[68:69] op_sel_hi:[1,0]
	v_pk_mul_f32 v[52:53], v[20:21], v[68:69] op_sel_hi:[1,0]
	v_pk_mul_f32 v[54:55], v[22:23], v[68:69] op_sel_hi:[1,0]
	v_pk_mul_f32 v[56:57], v[24:25], v[68:69] op_sel_hi:[1,0]
	v_pk_mul_f32 v[18:19], v[42:43], v[28:29] op_sel_hi:[1,0]
	v_pk_mul_f32 v[20:21], v[44:45], v[28:29] op_sel_hi:[1,0]
	v_pk_mul_f32 v[22:23], v[46:47], v[28:29] op_sel_hi:[1,0]
	v_pk_mul_f32 v[26:27], v[48:49], v[28:29] op_sel_hi:[1,0]
	v_pk_mul_f32 v[162:163], v[34:35], v[28:29] op_sel_hi:[1,0]
	v_pk_mul_f32 v[164:165], v[36:37], v[28:29] op_sel_hi:[1,0]
	v_pk_mul_f32 v[166:167], v[38:39], v[28:29] op_sel_hi:[1,0]
	v_pk_mul_f32 v[24:25], v[40:41], v[28:29] op_sel_hi:[1,0]
	v_pk_mul_f32 v[104:105], v[2:3], v[28:29] op_sel_hi:[1,0]
	v_pk_mul_f32 v[112:113], v[4:5], v[28:29] op_sel_hi:[1,0]
	ds_read_b128 v[2:5], v150 offset:60416
	ds_read_b128 v[34:37], v174 offset:32768
	ds_read_b128 v[38:41], v174 offset:32800
	ds_read_b128 v[42:45], v174 offset:32832
	ds_read_b128 v[46:49], v174 offset:32864
	v_cvt_pk_bf16_f32 v129, v168, v169
	v_cvt_pk_bf16_f32 v128, v82, v83
	v_cvt_pk_bf16_f32 v127, v160, v161
	v_cvt_pk_bf16_f32 v126, v158, v159
	v_cvt_pk_bf16_f32 v137, v24, v25
	v_cvt_pk_bf16_f32 v136, v166, v167
	v_cvt_pk_bf16_f32 v135, v164, v165
	s_waitcnt lgkmcnt(0)
	v_mfma_f32_32x32x16_bf16 v[86:101], v[2:5], v[126:129], v[34:49]
	v_cvt_pk_bf16_f32 v134, v162, v163
	v_mul_f32_e32 v84, v62, v68
	v_mul_f32_e32 v85, v63, v68
	v_mul_f32_e32 v170, v64, v68
	v_mul_f32_e32 v171, v65, v68
	v_pk_mul_f32 v[62:63], v[30:31], v[68:69] op_sel_hi:[1,0]
	v_pk_mul_f32 v[64:65], v[32:33], v[68:69] op_sel_hi:[1,0]
	v_pk_mul_f32 v[116:117], v[6:7], v[28:29] op_sel_hi:[1,0]
	v_pk_mul_f32 v[154:155], v[8:9], v[28:29] op_sel_hi:[1,0]
	v_mfma_f32_32x32x16_bf16 v[34:49], v[2:5], v[134:137], v[34:49]
	ds_read_b128 v[6:9], v150 offset:61440
	ds_read_b128 v[66:69], v174 offset:32896
	ds_read_b128 v[106:109], v150 offset:64512
	v_cvt_pk_bf16_f32 v125, v170, v171
	v_cvt_pk_bf16_f32 v124, v84, v85
	v_cvt_pk_bf16_f32 v123, v80, v81
	v_cvt_pk_bf16_f32 v122, v78, v79
	v_cvt_pk_bf16_f32 v149, v26, v27
	v_cvt_pk_bf16_f32 v148, v22, v23
	v_cvt_pk_bf16_f32 v147, v20, v21
	v_cvt_pk_bf16_f32 v146, v18, v19
	s_waitcnt lgkmcnt(2)
	v_mfma_f32_32x32x16_bf16 v[86:101], v[6:9], v[122:125], v[86:101]
	v_mul_f32_e32 v102, v10, v28
	v_mul_f32_e32 v103, v11, v28
	v_mul_f32_e32 v110, v12, v28
	v_mul_f32_e32 v111, v13, v28
	v_mul_f32_e32 v114, v14, v28
	v_mul_f32_e32 v115, v15, v28
	v_pk_mul_f32 v[156:157], v[16:17], v[28:29] op_sel_hi:[1,0]
	ds_read_b128 v[176:179], v174 offset:33536
	ds_read_b128 v[180:183], v174 offset:33568
	ds_read_b128 v[184:187], v174 offset:33600
	ds_read_b128 v[28:31], v174 offset:33632
	ds_read_b128 v[188:191], v174 offset:33792
	ds_read_b128 v[192:195], v174 offset:33824
	ds_read_b128 v[196:199], v174 offset:33856
	ds_read_b128 v[200:203], v174 offset:33888
	ds_read_b128 v[204:207], v150 offset:62464
	v_cvt_pk_bf16_f32 v133, v56, v57
	v_mfma_f32_32x32x16_bf16 v[34:49], v[6:9], v[146:149], v[34:49]
	v_cvt_pk_bf16_f32 v132, v54, v55
	v_cvt_pk_bf16_f32 v131, v52, v53
	v_cvt_pk_bf16_f32 v130, v50, v51
	ds_read_b128 v[70:73], v174 offset:33664
	ds_read_b128 v[74:77], v174 offset:33920
	ds_read_b128 v[208:211], v150 offset:63488
	v_cvt_pk_bf16_f32 v145, v154, v155
	v_cvt_pk_bf16_f32 v144, v116, v117
	v_cvt_pk_bf16_f32 v143, v112, v113
	v_cvt_pk_bf16_f32 v142, v104, v105
	s_waitcnt lgkmcnt(3)
	v_mfma_f32_32x32x16_bf16 v[86:101], v[204:207], v[130:133], v[86:101]
	v_cvt_pk_bf16_f32 v121, v64, v65
	v_cvt_pk_bf16_f32 v120, v62, v63
	v_cvt_pk_bf16_f32 v119, v60, v61
	v_cvt_pk_bf16_f32 v118, v58, v59
	v_cvt_pk_bf16_f32 v141, v156, v157
	v_cvt_pk_bf16_f32 v140, v114, v115
	v_cvt_pk_bf16_f32 v139, v110, v111
	v_mfma_f32_32x32x16_bf16 v[34:49], v[204:207], v[142:145], v[34:49]
	v_cvt_pk_bf16_f32 v138, v102, v103
	v_fma_f32 v16, v30, v170, v202
	v_fma_f32 v17, v31, v171, v203
	v_fma_f32 v14, v28, v84, v200
	v_fma_f32 v15, v29, v85, v201
	v_pk_fma_f32 v[12:13], v[186:187], v[80:81], v[198:199]
	v_pk_fma_f32 v[10:11], v[184:185], v[78:79], v[196:197]
	v_pk_fma_f32 v[8:9], v[182:183], v[168:169], v[194:195]
	s_waitcnt lgkmcnt(0)
	v_mfma_f32_32x32x16_bf16 v[86:101], v[208:211], v[118:121], v[86:101]
	v_fma_f32 v6, v180, v82, v192
	v_fma_f32 v7, v181, v83, v193
	ds_read_b128 v[78:81], v174 offset:33760
	ds_read_b128 v[82:85], v174 offset:33248
	v_fma_f32 v4, v178, v160, v190
	v_fma_f32 v5, v179, v161, v191
	v_pk_fma_f32 v[2:3], v[176:177], v[158:159], v[188:189]
	v_pk_fma_f32 v[32:33], v[30:31], v[26:27], v[202:203]
	v_pk_fma_f32 v[30:31], v[28:29], v[22:23], v[200:201]
	v_pk_fma_f32 v[28:29], v[186:187], v[20:21], v[198:199]
	v_pk_fma_f32 v[26:27], v[184:185], v[18:19], v[196:197]
	v_pk_fma_f32 v[24:25], v[182:183], v[24:25], v[194:195]
	v_pk_fma_f32 v[22:23], v[180:181], v[166:167], v[192:193]
	v_pk_fma_f32 v[20:21], v[178:179], v[164:165], v[190:191]
	v_pk_fma_f32 v[18:19], v[176:177], v[162:163], v[188:189]
	ds_read_b128 v[158:161], v174 offset:33696
	ds_read_b128 v[162:165], v174 offset:33728
	ds_read_b128 v[166:169], v174 offset:33952
	ds_read_b128 v[176:179], v174 offset:33984
	ds_read_b128 v[180:183], v174 offset:34016
	ds_read_b128 v[184:187], v212 offset:11264
	v_mfma_f32_32x32x16_bf16 v[34:49], v[208:211], v[138:141], v[34:49]
	v_cvt_pk_bf16_f32 v86, v86, v87
	v_cvt_pk_bf16_f32 v87, v88, v89
	v_cvt_pk_bf16_f32 v88, v90, v91
	v_cvt_pk_bf16_f32 v89, v92, v93
	ds_read_b128 v[90:93], v212 offset:12288
	v_pk_max_i16 v86, v86, 0
	v_pk_max_i16 v87, v87, 0
	v_pk_max_i16 v88, v88, 0
	v_pk_max_i16 v89, v89, 0
	s_nop 1
	s_nop 0
	v_cvt_pk_bf16_f32 v188, v34, v35
	v_cvt_pk_bf16_f32 v189, v36, v37
	v_cvt_pk_bf16_f32 v190, v38, v39
	v_cvt_pk_bf16_f32 v191, v40, v41
	s_waitcnt lgkmcnt(1)
	v_mfma_f32_32x32x16_bf16 v[2:17], v[184:187], v[86:89], v[2:17]
	v_pk_max_i16 v188, v188, 0
	v_pk_max_i16 v189, v189, 0
	v_pk_max_i16 v190, v190, 0
	v_pk_max_i16 v191, v191, 0
	v_cvt_pk_bf16_f32 v94, v94, v95
	v_cvt_pk_bf16_f32 v95, v96, v97
	v_cvt_pk_bf16_f32 v96, v98, v99
	v_cvt_pk_bf16_f32 v97, v100, v101
	v_cvt_pk_bf16_f32 v98, v42, v43
	v_cvt_pk_bf16_f32 v99, v44, v45
	v_mfma_f32_32x32x16_bf16 v[18:33], v[184:187], v[188:191], v[18:33]
	ds_read_b128 v[184:187], v212 offset:19456
	v_cvt_pk_bf16_f32 v100, v46, v47
	v_cvt_pk_bf16_f32 v101, v48, v49
	v_fma_f32 v64, v80, v64, v182
	v_fma_f32 v65, v81, v65, v183
	v_pk_fma_f32 v[62:63], v[78:79], v[62:63], v[180:181]
	v_pk_fma_f32 v[60:61], v[164:165], v[60:61], v[178:179]
	v_pk_fma_f32 v[58:59], v[162:163], v[58:59], v[176:177]
	v_pk_max_i16 v94, v94, 0
	v_pk_max_i16 v95, v95, 0
	v_pk_max_i16 v96, v96, 0
	v_pk_max_i16 v97, v97, 0
	v_pk_max_i16 v98, v98, 0
	v_pk_max_i16 v99, v99, 0
	v_pk_max_i16 v100, v100, 0
	v_pk_max_i16 v101, v101, 0
	v_pk_fma_f32 v[56:57], v[160:161], v[56:57], v[168:169]
	s_waitcnt lgkmcnt(1)
	v_mfma_f32_32x32x16_bf16 v[2:17], v[90:93], v[94:97], v[2:17]
	v_fma_f32 v54, v158, v54, v166
	v_fma_f32 v55, v159, v55, v167
	v_fma_f32 v52, v72, v52, v76
	v_fma_f32 v53, v73, v53, v77
	v_fma_f32 v50, v70, v50, v74
	v_fma_f32 v51, v71, v51, v75
	v_pk_fma_f32 v[48:49], v[80:81], v[156:157], v[182:183]
	v_pk_fma_f32 v[46:47], v[78:79], v[114:115], v[180:181]
	v_pk_fma_f32 v[44:45], v[164:165], v[110:111], v[178:179]
	v_pk_fma_f32 v[42:43], v[162:163], v[102:103], v[176:177]
	v_mfma_f32_32x32x16_bf16 v[18:33], v[90:93], v[98:101], v[18:33]
	ds_read_b128 v[90:93], v212 offset:20480
	v_fma_f32 v40, v160, v154, v168
	v_fma_f32 v41, v161, v155, v169
	v_fma_f32 v38, v158, v116, v166
	v_fma_f32 v39, v159, v117, v167
	v_pk_fma_f32 v[36:37], v[72:73], v[112:113], v[76:77]
	v_pk_fma_f32 v[34:35], v[70:71], v[104:105], v[74:75]
	s_waitcnt lgkmcnt(1)
	v_mfma_f32_32x32x16_bf16 v[50:65], v[184:187], v[86:89], v[50:65]
	ds_read_b128 v[70:73], v174 offset:32928
	ds_read_b128 v[74:77], v174 offset:32960
	ds_read_b128 v[78:81], v174 offset:32992
	ds_read_b128 v[86:89], v174 offset:33024
	ds_read_b128 v[110:113], v212 offset:1024
	v_mfma_f32_32x32x16_bf16 v[34:49], v[184:187], v[188:191], v[34:49]
	s_waitcnt lgkmcnt(5)
	v_mfma_f32_32x32x16_bf16 v[50:65], v[90:93], v[94:97], v[50:65]
	v_mfma_f32_32x32x16_bf16 v[34:49], v[90:93], v[98:101], v[34:49]
	s_waitcnt lgkmcnt(2)
	v_mfma_f32_32x32x16_bf16 v[90:105], v[106:109], v[126:129], v[66:81]
	v_mfma_f32_32x32x16_bf16 v[66:81], v[106:109], v[134:137], v[66:81]
	ds_read_b128 v[106:109], v212 offset:0
	s_waitcnt lgkmcnt(0)
	v_mfma_f32_32x32x16_bf16 v[90:105], v[106:109], v[122:125], v[90:105]
	v_mfma_f32_32x32x16_bf16 v[66:81], v[106:109], v[146:149], v[66:81]
	ds_read_b128 v[106:109], v212 offset:2048
	v_mfma_f32_32x32x16_bf16 v[90:105], v[110:113], v[130:133], v[90:105]
	v_mfma_f32_32x32x16_bf16 v[66:81], v[110:113], v[142:145], v[66:81]
	ds_read_b128 v[110:113], v212 offset:13312
	s_waitcnt lgkmcnt(1)
	v_mfma_f32_32x32x16_bf16 v[90:105], v[106:109], v[118:121], v[90:105]
	v_mfma_f32_32x32x16_bf16 v[66:81], v[106:109], v[138:141], v[66:81]
	s_nop 10
	v_cvt_pk_bf16_f32 v90, v90, v91
	v_cvt_pk_bf16_f32 v91, v92, v93
	v_cvt_pk_bf16_f32 v92, v94, v95
	v_cvt_pk_bf16_f32 v94, v98, v99
	v_cvt_pk_bf16_f32 v95, v100, v101
	ds_read_b128 v[98:101], v212 offset:21504
	v_cvt_pk_bf16_f32 v66, v66, v67
	v_cvt_pk_bf16_f32 v67, v68, v69
	v_cvt_pk_bf16_f32 v68, v70, v71
	v_cvt_pk_bf16_f32 v93, v96, v97
	v_cvt_pk_bf16_f32 v69, v72, v73
	ds_read_b128 v[70:73], v212 offset:14336
	v_pk_max_i16 v90, v90, 0
	v_pk_max_i16 v91, v91, 0
	v_pk_max_i16 v92, v92, 0
	v_pk_max_i16 v93, v93, 0
	v_pk_max_i16 v66, v66, 0
	v_pk_max_i16 v67, v67, 0
	v_pk_max_i16 v68, v68, 0
	v_pk_max_i16 v69, v69, 0
	v_cvt_pk_bf16_f32 v96, v102, v103
	s_waitcnt lgkmcnt(2)
	v_mfma_f32_32x32x16_bf16 v[2:17], v[110:113], v[90:93], v[2:17]
	v_cvt_pk_bf16_f32 v97, v104, v105
	v_cvt_pk_bf16_f32 v74, v74, v75
	v_cvt_pk_bf16_f32 v75, v76, v77
	v_cvt_pk_bf16_f32 v76, v78, v79
	v_cvt_pk_bf16_f32 v77, v80, v81
	v_pk_max_i16 v94, v94, 0
	v_pk_max_i16 v95, v95, 0
	v_pk_max_i16 v96, v96, 0
	v_pk_max_i16 v97, v97, 0
	v_pk_max_i16 v74, v74, 0
	v_pk_max_i16 v75, v75, 0
	v_pk_max_i16 v76, v76, 0
	v_pk_max_i16 v77, v77, 0
	v_mfma_f32_32x32x16_bf16 v[18:33], v[110:113], v[66:69], v[18:33]
	s_waitcnt lgkmcnt(1)
	v_mfma_f32_32x32x16_bf16 v[34:49], v[98:101], v[66:69], v[34:49]
	ds_read_b128 v[66:69], v212 offset:22528
	v_mfma_f32_32x32x16_bf16 v[50:65], v[98:101], v[90:93], v[50:65]
	s_waitcnt lgkmcnt(1)
	v_mfma_f32_32x32x16_bf16 v[2:17], v[70:73], v[94:97], v[2:17]
	v_mfma_f32_32x32x16_bf16 v[18:33], v[70:73], v[74:77], v[18:33]
	ds_read_b128 v[78:81], v212 offset:3072
	s_waitcnt lgkmcnt(1)
	v_mfma_f32_32x32x16_bf16 v[50:65], v[66:69], v[94:97], v[50:65]
	ds_read_b128 v[90:93], v174 offset:33056
	ds_read_b128 v[94:97], v174 offset:33088
	ds_read_b128 v[98:101], v174 offset:33120
	ds_read_b128 v[70:73], v174 offset:33152
	v_mfma_f32_32x32x16_bf16 v[34:49], v[66:69], v[74:77], v[34:49]
	ds_read_b128 v[66:69], v212 offset:4096
	ds_read_b128 v[74:77], v212 offset:5120
	s_waitcnt lgkmcnt(3)
	v_mfma_f32_32x32x16_bf16 v[102:117], v[78:81], v[126:129], v[86:101]
	v_mfma_f32_32x32x16_bf16 v[86:101], v[78:81], v[134:137], v[86:101]
	s_waitcnt lgkmcnt(1)
	v_mfma_f32_32x32x16_bf16 v[86:101], v[66:69], v[146:149], v[86:101]
	v_mfma_f32_32x32x16_bf16 v[102:117], v[66:69], v[122:125], v[102:117]
	ds_read_b128 v[66:69], v212 offset:6144
	s_waitcnt lgkmcnt(1)
	v_mfma_f32_32x32x16_bf16 v[86:101], v[74:77], v[142:145], v[86:101]
	v_mfma_f32_32x32x16_bf16 v[102:117], v[74:77], v[130:133], v[102:117]
	ds_read_b128 v[74:77], v212 offset:15360
	s_waitcnt lgkmcnt(1)
	v_mfma_f32_32x32x16_bf16 v[86:101], v[66:69], v[138:141], v[86:101]
	v_mfma_f32_32x32x16_bf16 v[102:117], v[66:69], v[118:121], v[102:117]
	s_nop 10
	v_cvt_pk_bf16_f32 v78, v86, v87
	v_cvt_pk_bf16_f32 v80, v90, v91
	v_cvt_pk_bf16_f32 v79, v88, v89
	v_cvt_pk_bf16_f32 v81, v92, v93
	ds_read_b128 v[86:89], v212 offset:16384
	ds_read_b128 v[90:93], v212 offset:23552
	v_cvt_pk_bf16_f32 v66, v102, v103
	v_cvt_pk_bf16_f32 v67, v104, v105
	v_cvt_pk_bf16_f32 v68, v106, v107
	v_cvt_pk_bf16_f32 v69, v108, v109
	v_pk_max_i16 v66, v66, 0
	v_pk_max_i16 v67, v67, 0
	v_pk_max_i16 v68, v68, 0
	v_pk_max_i16 v69, v69, 0
	v_pk_max_i16 v78, v78, 0
	v_pk_max_i16 v79, v79, 0
	v_pk_max_i16 v80, v80, 0
	v_pk_max_i16 v81, v81, 0
	v_cvt_pk_bf16_f32 v94, v94, v95
	s_waitcnt lgkmcnt(2)
	v_mfma_f32_32x32x16_bf16 v[18:33], v[74:77], v[78:81], v[18:33]
	v_cvt_pk_bf16_f32 v95, v96, v97
	v_cvt_pk_bf16_f32 v96, v98, v99
	v_cvt_pk_bf16_f32 v97, v100, v101
	v_pk_max_i16 v94, v94, 0
	v_pk_max_i16 v95, v95, 0
	v_pk_max_i16 v96, v96, 0
	v_pk_max_i16 v97, v97, 0
	v_mfma_f32_32x32x16_bf16 v[2:17], v[74:77], v[66:69], v[2:17]
	v_cvt_pk_bf16_f32 v74, v110, v111
	v_cvt_pk_bf16_f32 v75, v112, v113
	v_cvt_pk_bf16_f32 v76, v114, v115
	v_cvt_pk_bf16_f32 v77, v116, v117
	v_pk_max_i16 v74, v74, 0
	v_pk_max_i16 v75, v75, 0
	v_pk_max_i16 v76, v76, 0
	v_pk_max_i16 v77, v77, 0
	s_waitcnt lgkmcnt(0)
	v_mfma_f32_32x32x16_bf16 v[50:65], v[90:93], v[66:69], v[50:65]
	ds_read_b128 v[66:69], v212 offset:24576
	v_mfma_f32_32x32x16_bf16 v[34:49], v[90:93], v[78:81], v[34:49]
	ds_read_b128 v[102:105], v212 offset:7168
	v_mfma_f32_32x32x16_bf16 v[2:17], v[86:89], v[74:77], v[2:17]
	s_waitcnt lgkmcnt(1)
	v_mfma_f32_32x32x16_bf16 v[50:65], v[66:69], v[74:77], v[50:65]
	ds_read_b128 v[74:77], v174 offset:33184
	ds_read_b128 v[78:81], v174 offset:33216
	v_mfma_f32_32x32x16_bf16 v[34:49], v[66:69], v[94:97], v[34:49]
	ds_read_b128 v[66:69], v212 offset:8192
	v_mfma_f32_32x32x16_bf16 v[18:33], v[86:89], v[94:97], v[18:33]
	s_waitcnt lgkmcnt(1)
	v_mfma_f32_32x32x16_bf16 v[86:101], v[102:105], v[126:129], v[70:85]
	v_mfma_f32_32x32x16_bf16 v[70:85], v[102:105], v[134:137], v[70:85]
	ds_read_b128 v[102:105], v212 offset:9216
	v_lshlrev_b32_e32 v135, 2, v1
	v_add_u32_e32 v134, v172, v174
	s_waitcnt lgkmcnt(1)
	v_mfma_f32_32x32x16_bf16 v[86:101], v[66:69], v[122:125], v[86:101]
	v_mfma_f32_32x32x16_bf16 v[70:85], v[66:69], v[146:149], v[70:85]
	ds_read_b128 v[66:69], v212 offset:10240
	s_waitcnt lgkmcnt(1)
	v_mfma_f32_32x32x16_bf16 v[86:101], v[102:105], v[130:133], v[86:101]
	v_mfma_f32_32x32x16_bf16 v[70:85], v[102:105], v[142:145], v[70:85]
	ds_read_b128 v[102:105], v212 offset:17408
	s_waitcnt lgkmcnt(1)
	v_mfma_f32_32x32x16_bf16 v[86:101], v[66:69], v[118:121], v[86:101]
	v_mfma_f32_32x32x16_bf16 v[70:85], v[66:69], v[138:141], v[70:85]
	s_nop 10
	v_cvt_pk_bf16_f32 v68, v90, v91
	v_cvt_pk_bf16_f32 v69, v92, v93
	ds_read_b128 v[90:93], v212 offset:25600
	v_cvt_pk_bf16_f32 v66, v86, v87
	v_cvt_pk_bf16_f32 v67, v88, v89
	v_pk_max_i16 v66, v66, 0
	v_pk_max_i16 v67, v67, 0
	v_pk_max_i16 v68, v68, 0
	v_pk_max_i16 v69, v69, 0
	v_cvt_pk_bf16_f32 v70, v70, v71
	v_cvt_pk_bf16_f32 v71, v72, v73
	s_waitcnt lgkmcnt(1)
	v_mfma_f32_32x32x16_bf16 v[2:17], v[102:105], v[66:69], v[2:17]
	v_cvt_pk_bf16_f32 v72, v74, v75
	v_cvt_pk_bf16_f32 v73, v76, v77
	ds_read_b128 v[74:77], v212 offset:18432
	v_cvt_pk_bf16_f32 v86, v94, v95
	v_cvt_pk_bf16_f32 v87, v96, v97
	v_cvt_pk_bf16_f32 v88, v98, v99
	s_waitcnt lgkmcnt(1)
	v_mfma_f32_32x32x16_bf16 v[50:65], v[90:93], v[66:69], v[50:65]
	ds_read_b128 v[66:69], v212 offset:26624
	v_cvt_pk_bf16_f32 v89, v100, v101
	v_pk_max_i16 v86, v86, 0
	v_pk_max_i16 v87, v87, 0
	v_pk_max_i16 v88, v88, 0
	v_pk_max_i16 v89, v89, 0
	v_pk_max_i16 v70, v70, 0
	v_pk_max_i16 v71, v71, 0
	v_pk_max_i16 v72, v72, 0
	v_pk_max_i16 v73, v73, 0
	v_cvt_pk_bf16_f32 v78, v78, v79
	v_cvt_pk_bf16_f32 v79, v80, v81
	s_waitcnt lgkmcnt(1)
	v_mfma_f32_32x32x16_bf16 v[2:17], v[74:77], v[86:89], v[2:17]
	v_cvt_pk_bf16_f32 v80, v82, v83
	v_cvt_pk_bf16_f32 v81, v84, v85
	v_pk_max_i16 v78, v78, 0
	v_pk_max_i16 v79, v79, 0
	v_pk_max_i16 v80, v80, 0
	v_pk_max_i16 v81, v81, 0
	s_waitcnt lgkmcnt(0)
	v_mfma_f32_32x32x16_bf16 v[50:65], v[66:69], v[86:89], v[50:65]
	v_mfma_f32_32x32x16_bf16 v[34:49], v[90:93], v[70:73], v[34:49]
	s_nop 10
	v_add_f32_e32 v130, v10, v58
	v_add_f32_e32 v131, v11, v59
	v_add_f32_e32 v132, v12, v60
	v_add_f32_e32 v133, v13, v61
	v_add_f32_e32 v138, v4, v52
	v_add_f32_e32 v139, v5, v53
	v_pk_add_f32 v[140:141], v[16:17], v[64:65]
	v_pk_add_f32 v[142:143], v[8:9], v[56:57]
	v_pk_add_f32 v[144:145], v[14:15], v[62:63]
	v_pk_add_f32 v[146:147], v[6:7], v[54:55]
	v_mfma_f32_32x32x16_bf16 v[18:33], v[102:105], v[70:73], v[18:33]
	ds_read2st64_b32 v[70:71], v135 offset0:133 offset1:134
	v_add_f32_e32 v148, v2, v50
	v_add_f32_e32 v149, v3, v51
	v_add_f32_e32 v144, v146, v144
	v_add_f32_e32 v145, v147, v145
	v_pk_add_f32 v[140:141], v[142:143], v[140:141]
	v_pk_add_f32 v[132:133], v[138:139], v[132:133]
	v_pk_add_f32 v[130:131], v[148:149], v[130:131]
	v_pk_add_f32 v[132:133], v[132:133], v[140:141]
	v_pk_add_f32 v[130:131], v[130:131], v[144:145]
	v_mfma_f32_32x32x16_bf16 v[34:49], v[66:69], v[78:81], v[34:49]
	v_pk_mov_b32 v[138:139], v[130:131], v[132:133] op_sel:[1,0]
	v_mov_b32_e32 v131, v133
	s_waitcnt vmcnt(0) lgkmcnt(0)
	v_mul_f32_e32 v66, v175, v70
	v_pk_add_f32 v[130:131], v[138:139], v[130:131]
	ds_write_b32 v173, v66 offset:512
	v_mul_f32_e32 v66, v175, v71
	v_pk_add_f32 v[130:131], v[130:131], v[130:131] op_sel:[0,1] op_sel_hi:[1,0]
	s_waitcnt lgkmcnt(0)
	ds_read_b128 v[102:105], v174 offset:34560
	ds_read_b128 v[98:101], v174 offset:34592
	ds_read_b128 v[110:113], v174 offset:34624
	ds_read_b128 v[106:109], v174 offset:34656
	ds_read_b128 v[114:117], v174 offset:34688
	ds_read_b128 v[122:125], v174 offset:34720
	ds_read_b128 v[118:121], v174 offset:34752
	ds_read_b128 v[126:129], v174 offset:34784
	v_mov_b32_dpp v66, v66 quad_perm:[1,0,3,2] row_mask:0xf bank_mask:0xf bound_ctrl:1
	v_mov_b32_e32 v131, v130
	v_fmac_f32_e32 v66, v175, v71
	s_nop 0
	v_permlane32_swap_b32_e32 v130, v131
	v_add_f32_dpp v66, v66, v66 quad_perm:[2,3,0,1] row_mask:0xf bank_mask:0xf bound_ctrl:1
	v_add_f32_e32 v130, v130, v131
	v_fmamk_f32 v65, v130, 0xbc800000, v65
	v_add_f32_dpp v66, v66, v66 row_half_mirror row_mask:0xf bank_mask:0xf bound_ctrl:1
	v_fmamk_f32 v64, v130, 0xbc800000, v64
	v_fmamk_f32 v63, v130, 0xbc800000, v63
	v_fmamk_f32 v62, v130, 0xbc800000, v62
	v_fmamk_f32 v61, v130, 0xbc800000, v61
	v_fmamk_f32 v60, v130, 0xbc800000, v60
	v_fmamk_f32 v59, v130, 0xbc800000, v59
	v_fmamk_f32 v58, v130, 0xbc800000, v58
	v_fmamk_f32 v57, v130, 0xbc800000, v57
	v_fmamk_f32 v56, v130, 0xbc800000, v56
	v_fmamk_f32 v55, v130, 0xbc800000, v55
	v_fmamk_f32 v54, v130, 0xbc800000, v54
	v_fmamk_f32 v53, v130, 0xbc800000, v53
	v_fmamk_f32 v52, v130, 0xbc800000, v52
	v_fmamk_f32 v51, v130, 0xbc800000, v51
	v_fmac_f32_e32 v50, 0xbc800000, v130
	v_add_f32_dpp v66, v66, v66 row_ror:8 row_mask:0xf bank_mask:0xf bound_ctrl:1
	v_fmamk_f32 v17, v130, 0xbc800000, v17
	v_fmamk_f32 v16, v130, 0xbc800000, v16
	v_fmamk_f32 v15, v130, 0xbc800000, v15
	v_fmamk_f32 v14, v130, 0xbc800000, v14
	v_fmamk_f32 v13, v130, 0xbc800000, v13
	v_fmamk_f32 v12, v130, 0xbc800000, v12
	v_fmamk_f32 v11, v130, 0xbc800000, v11
	v_fmamk_f32 v10, v130, 0xbc800000, v10
	v_fmamk_f32 v9, v130, 0xbc800000, v9
	v_fmamk_f32 v8, v130, 0xbc800000, v8
	v_fmamk_f32 v7, v130, 0xbc800000, v7
	v_fmamk_f32 v6, v130, 0xbc800000, v6
	v_fmamk_f32 v5, v130, 0xbc800000, v5
	v_fmamk_f32 v4, v130, 0xbc800000, v4
	v_fmamk_f32 v3, v130, 0xbc800000, v3
	v_fmac_f32_e32 v2, 0xbc800000, v130
	v_pk_mul_f32 v[130:131], v[54:55], v[54:55]
	v_pk_mul_f32 v[132:133], v[62:63], v[62:63]
	v_pk_mul_f32 v[138:139], v[50:51], v[50:51]
	v_pk_mul_f32 v[140:141], v[58:59], v[58:59]
	v_pk_mul_f32 v[142:143], v[56:57], v[56:57]
	v_pk_mul_f32 v[144:145], v[64:65], v[64:65]
	v_pk_mul_f32 v[146:147], v[52:53], v[52:53]
	v_pk_mul_f32 v[148:149], v[60:61], v[60:61]
	v_mov_b32_e32 v67, v66
	v_pk_fma_f32 v[148:149], v[12:13], v[12:13], v[148:149]
	v_pk_fma_f32 v[146:147], v[4:5], v[4:5], v[146:147]
	v_pk_fma_f32 v[144:145], v[16:17], v[16:17], v[144:145]
	v_pk_fma_f32 v[142:143], v[8:9], v[8:9], v[142:143]
	v_pk_fma_f32 v[140:141], v[10:11], v[10:11], v[140:141]
	v_pk_fma_f32 v[138:139], v[2:3], v[2:3], v[138:139]
	v_pk_fma_f32 v[132:133], v[14:15], v[14:15], v[132:133]
	v_pk_fma_f32 v[130:131], v[6:7], v[6:7], v[130:131]
	v_permlane16_swap_b32_e32 v66, v67
	v_pk_add_f32 v[130:131], v[130:131], v[132:133]
	v_pk_add_f32 v[132:133], v[138:139], v[140:141]
	v_pk_add_f32 v[138:139], v[142:143], v[144:145]
	v_pk_add_f32 v[140:141], v[146:147], v[148:149]
	v_mfma_f32_32x32x16_bf16 v[18:33], v[74:77], v[78:81], v[18:33]
	v_add_f32_e32 v136, v66, v67
	ds_read_b128 v[70:73], v134 offset:512
	ds_read_b128 v[66:69], v134 offset:544
	ds_read_b128 v[78:81], v134 offset:576
	ds_read_b128 v[74:77], v134 offset:608
	ds_read_b128 v[82:85], v134 offset:640
	ds_read_b128 v[90:93], v134 offset:672
	ds_read_b128 v[86:89], v134 offset:704
	ds_read_b128 v[94:97], v134 offset:736
	v_pk_add_f32 v[138:139], v[140:141], v[138:139]
	v_pk_add_f32 v[130:131], v[132:133], v[130:131]
	s_waitcnt lgkmcnt(8)
	v_pk_mul_f32 v[140:141], v[126:127], v[62:63]
	v_pk_mov_b32 v[132:133], v[130:131], v[138:139] op_sel:[1,0]
	v_mov_b32_e32 v131, v139
	v_pk_mul_f32 v[138:139], v[122:123], v[54:55]
	v_pk_mul_f32 v[142:143], v[114:115], v[50:51]
	v_pk_mul_f32 v[144:145], v[118:119], v[58:59]
	v_pk_mul_f32 v[146:147], v[124:125], v[56:57]
	v_pk_mul_f32 v[148:149], v[128:129], v[64:65]
	v_pk_mul_f32 v[154:155], v[116:117], v[52:53]
	v_pk_mul_f32 v[156:157], v[120:121], v[60:61]
	v_pk_fma_f32 v[154:155], v[104:105], v[4:5], v[154:155]
	v_pk_fma_f32 v[156:157], v[112:113], v[12:13], v[156:157]
	v_pk_fma_f32 v[148:149], v[108:109], v[16:17], v[148:149]
	v_pk_fma_f32 v[146:147], v[100:101], v[8:9], v[146:147]
	v_pk_fma_f32 v[144:145], v[110:111], v[10:11], v[144:145]
	v_pk_fma_f32 v[142:143], v[102:103], v[2:3], v[142:143]
	v_pk_fma_f32 v[140:141], v[106:107], v[14:15], v[140:141]
	v_pk_fma_f32 v[138:139], v[98:99], v[6:7], v[138:139]
	v_pk_add_f32 v[130:131], v[132:133], v[130:131]
	v_pk_add_f32 v[138:139], v[138:139], v[140:141]
	v_pk_add_f32 v[140:141], v[142:143], v[144:145]
	v_pk_add_f32 v[142:143], v[146:147], v[148:149]
	v_pk_add_f32 v[144:145], v[154:155], v[156:157]
	v_pk_add_f32 v[132:133], v[130:131], v[130:131] op_sel:[0,1] op_sel_hi:[1,0]
	v_pk_add_f32 v[142:143], v[144:145], v[142:143]
	v_pk_add_f32 v[138:139], v[140:141], v[138:139]
	v_add_f32_e32 v133, v142, v143
	v_add_f32_e32 v130, v138, v139
	s_waitcnt lgkmcnt(2)
	v_pk_mul_f32 v[138:139], v[90:91], v[54:55]
	s_waitcnt lgkmcnt(0)
	v_pk_mul_f32 v[140:141], v[94:95], v[62:63]
	v_pk_mul_f32 v[142:143], v[82:83], v[50:51]
	v_pk_mul_f32 v[144:145], v[86:87], v[58:59]
	v_pk_mul_f32 v[146:147], v[92:93], v[56:57]
	v_pk_mul_f32 v[148:149], v[96:97], v[64:65]
	v_pk_mul_f32 v[154:155], v[84:85], v[52:53]
	v_pk_mul_f32 v[156:157], v[88:89], v[60:61]
	v_add_f32_e32 v130, v130, v133
	v_pk_fma_f32 v[156:157], v[80:81], v[12:13], v[156:157]
	v_pk_fma_f32 v[154:155], v[72:73], v[4:5], v[154:155]
	v_pk_fma_f32 v[148:149], v[76:77], v[16:17], v[148:149]
	v_pk_fma_f32 v[146:147], v[68:69], v[8:9], v[146:147]
	v_pk_fma_f32 v[144:145], v[78:79], v[10:11], v[144:145]
	v_pk_fma_f32 v[142:143], v[70:71], v[2:3], v[142:143]
	v_pk_fma_f32 v[140:141], v[74:75], v[14:15], v[140:141]
	v_pk_fma_f32 v[138:139], v[66:67], v[6:7], v[138:139]
	v_mov_b32_e32 v133, v130
	v_pk_add_f32 v[138:139], v[138:139], v[140:141]
	v_pk_add_f32 v[140:141], v[142:143], v[144:145]
	v_pk_add_f32 v[142:143], v[146:147], v[148:149]
	v_pk_add_f32 v[144:145], v[154:155], v[156:157]
	v_permlane32_swap_b32_e32 v130, v133
	v_pk_add_f32 v[142:143], v[144:145], v[142:143]
	v_add_f32_e32 v160, v130, v133
	v_pk_add_f32 v[138:139], v[140:141], v[138:139]
	v_add_f32_e32 v133, v142, v143
	v_pk_add_f32 v[140:141], v[26:27], v[42:43]
	v_pk_add_f32 v[142:143], v[28:29], v[44:45]
	v_pk_add_f32 v[144:145], v[20:21], v[36:37]
	v_pk_add_f32 v[146:147], v[32:33], v[48:49]
	v_pk_add_f32 v[148:149], v[24:25], v[40:41]
	v_pk_add_f32 v[154:155], v[30:31], v[46:47]
	v_pk_add_f32 v[156:157], v[22:23], v[38:39]
	v_pk_add_f32 v[158:159], v[18:19], v[34:35]
	v_pk_add_f32 v[154:155], v[156:157], v[154:155]
	v_pk_add_f32 v[146:147], v[148:149], v[146:147]
	v_pk_add_f32 v[142:143], v[144:145], v[142:143]
	v_pk_add_f32 v[140:141], v[158:159], v[140:141]
	v_pk_add_f32 v[142:143], v[142:143], v[146:147]
	v_pk_add_f32 v[140:141], v[140:141], v[154:155]
	v_add_f32_e32 v130, v138, v139
	v_pk_mov_b32 v[144:145], v[140:141], v[142:143] op_sel:[1,0]
	v_mov_b32_e32 v141, v143
	v_pk_add_f32 v[140:141], v[144:145], v[140:141]
	v_add_f32_e32 v133, v130, v133
	v_pk_add_f32 v[140:141], v[140:141], v[140:141] op_sel:[0,1] op_sel_hi:[1,0]
	v_mov_b32_e32 v131, v132
	v_mov_b32_e32 v130, v140
	s_nop 1
	v_permlane32_swap_b32_e32 v140, v130
	v_add_f32_e32 v130, v140, v130
	v_fmamk_f32 v49, v130, 0xbc800000, v49
	v_fmamk_f32 v48, v130, 0xbc800000, v48
	v_fmamk_f32 v47, v130, 0xbc800000, v47
	v_fmamk_f32 v46, v130, 0xbc800000, v46
	v_fmamk_f32 v45, v130, 0xbc800000, v45
	v_fmamk_f32 v44, v130, 0xbc800000, v44
	v_fmamk_f32 v43, v130, 0xbc800000, v43
	v_fmamk_f32 v42, v130, 0xbc800000, v42
	v_fmamk_f32 v41, v130, 0xbc800000, v41
	v_fmamk_f32 v40, v130, 0xbc800000, v40
	v_fmamk_f32 v39, v130, 0xbc800000, v39
	v_fmamk_f32 v38, v130, 0xbc800000, v38
	v_fmamk_f32 v37, v130, 0xbc800000, v37
	v_fmamk_f32 v36, v130, 0xbc800000, v36
	v_fmamk_f32 v35, v130, 0xbc800000, v35
	v_fmac_f32_e32 v34, 0xbc800000, v130
	v_fmamk_f32 v33, v130, 0xbc800000, v33
	v_fmamk_f32 v32, v130, 0xbc800000, v32
	v_fmamk_f32 v31, v130, 0xbc800000, v31
	v_fmamk_f32 v30, v130, 0xbc800000, v30
	v_fmamk_f32 v29, v130, 0xbc800000, v29
	v_fmamk_f32 v28, v130, 0xbc800000, v28
	v_fmamk_f32 v27, v130, 0xbc800000, v27
	v_fmamk_f32 v26, v130, 0xbc800000, v26
	v_fmamk_f32 v25, v130, 0xbc800000, v25
	v_fmamk_f32 v24, v130, 0xbc800000, v24
	v_fmamk_f32 v23, v130, 0xbc800000, v23
	v_fmamk_f32 v22, v130, 0xbc800000, v22
	v_fmamk_f32 v21, v130, 0xbc800000, v21
	v_fmamk_f32 v20, v130, 0xbc800000, v20
	v_fmamk_f32 v19, v130, 0xbc800000, v19
	v_fmac_f32_e32 v18, 0xbc800000, v130
	v_pk_mul_f32 v[140:141], v[38:39], v[38:39]
	v_pk_mul_f32 v[142:143], v[46:47], v[46:47]
	v_pk_mul_f32 v[144:145], v[34:35], v[34:35]
	v_pk_mul_f32 v[146:147], v[42:43], v[42:43]
	v_pk_mul_f32 v[148:149], v[40:41], v[40:41]
	v_pk_mul_f32 v[154:155], v[48:49], v[48:49]
	v_pk_mul_f32 v[156:157], v[36:37], v[36:37]
	v_pk_mul_f32 v[158:159], v[44:45], v[44:45]
	v_pk_fma_f32 v[156:157], v[20:21], v[20:21], v[156:157]
	v_pk_fma_f32 v[158:159], v[28:29], v[28:29], v[158:159]
	v_pk_fma_f32 v[154:155], v[32:33], v[32:33], v[154:155]
	v_pk_fma_f32 v[148:149], v[24:25], v[24:25], v[148:149]
	v_pk_fma_f32 v[146:147], v[26:27], v[26:27], v[146:147]
	v_pk_fma_f32 v[144:145], v[18:19], v[18:19], v[144:145]
	v_pk_fma_f32 v[142:143], v[30:31], v[30:31], v[142:143]
	v_pk_fma_f32 v[140:141], v[22:23], v[22:23], v[140:141]
	v_permlane32_swap_b32_e32 v132, v131
	v_pk_add_f32 v[140:141], v[140:141], v[142:143]
	v_pk_add_f32 v[142:143], v[144:145], v[146:147]
	v_pk_add_f32 v[144:145], v[148:149], v[154:155]
	v_pk_add_f32 v[146:147], v[156:157], v[158:159]
	v_pk_add_f32 v[140:141], v[142:143], v[140:141]
	v_pk_add_f32 v[144:145], v[146:147], v[144:145]
	v_pk_mul_f32 v[122:123], v[122:123], v[38:39]
	v_pk_mov_b32 v[142:143], v[140:141], v[144:145] op_sel:[1,0]
	v_mov_b32_e32 v141, v145
	v_pk_add_f32 v[140:141], v[142:143], v[140:141]
	v_pk_mul_f32 v[126:127], v[126:127], v[46:47]
	v_pk_add_f32 v[140:141], v[140:141], v[140:141] op_sel:[0,1] op_sel_hi:[1,0]
	v_pk_mul_f32 v[114:115], v[114:115], v[34:35]
	v_mov_b32_e32 v130, v140
	s_nop 1
	v_permlane32_swap_b32_e32 v140, v130
	v_mov_b32_e32 v141, v132
	v_pk_add_f32 v[130:131], v[140:141], v[130:131]
	v_pk_mul_f32 v[118:119], v[118:119], v[42:43]
	v_pk_fma_f32 v[130:131], v[130:131], s[0:1], v[152:153] op_sel_hi:[1,0,0]
	v_pk_mul_f32 v[124:125], v[124:125], v[40:41]
	v_mul_f32_e32 v132, 0x4b800000, v131
	v_cmp_gt_f32_e32 vcc, s1, v131
	v_pk_mul_f32 v[128:129], v[128:129], v[48:49]
	v_pk_mul_f32 v[116:117], v[116:117], v[36:37]
	v_pk_mul_f32 v[120:121], v[120:121], v[44:45]
	v_cndmask_b32_e32 v131, v131, v132, vcc
	v_mul_f32_e32 v132, 0x4b800000, v130
	v_cmp_gt_f32_e64 s[0:1], s1, v130
	v_pk_fma_f32 v[112:113], v[112:113], v[28:29], v[120:121]
	v_pk_fma_f32 v[104:105], v[104:105], v[20:21], v[116:117]
	v_pk_fma_f32 v[108:109], v[108:109], v[32:33], v[128:129]
	v_pk_fma_f32 v[100:101], v[100:101], v[24:25], v[124:125]
	v_pk_fma_f32 v[110:111], v[110:111], v[26:27], v[118:119]
	v_pk_fma_f32 v[102:103], v[102:103], v[18:19], v[114:115]
	v_pk_fma_f32 v[106:107], v[106:107], v[30:31], v[126:127]
	v_pk_fma_f32 v[98:99], v[98:99], v[22:23], v[122:123]
	v_rsq_f32_e32 v131, v131
	v_cndmask_b32_e64 v130, v130, v132, s[0:1]
	v_pk_add_f32 v[98:99], v[98:99], v[106:107]
	v_pk_add_f32 v[102:103], v[102:103], v[110:111]
	v_pk_add_f32 v[100:101], v[100:101], v[108:109]
	v_pk_add_f32 v[104:105], v[104:105], v[112:113]
	v_rsq_f32_e32 v132, v130
	v_pk_add_f32 v[100:101], v[104:105], v[100:101]
	v_pk_add_f32 v[98:99], v[102:103], v[98:99]
	v_mul_f32_e32 v130, 0x45800000, v131
	v_add_f32_e32 v98, v98, v99
	v_add_f32_e32 v99, v100, v101
	v_add_f32_e32 v98, v98, v99
	v_mov_b32_e32 v99, v98
	v_pk_mul_f32 v[90:91], v[90:91], v[38:39]
	v_pk_mul_f32 v[94:95], v[94:95], v[46:47]
	v_pk_mul_f32 v[82:83], v[82:83], v[34:35]
	v_pk_mul_f32 v[86:87], v[86:87], v[42:43]
	v_cndmask_b32_e32 v130, v131, v130, vcc
	v_mul_f32_e32 v131, 0x45800000, v132
	v_permlane32_swap_b32_e32 v98, v99
	v_pk_fma_f32 v[78:79], v[78:79], v[26:27], v[86:87]
	v_pk_fma_f32 v[70:71], v[70:71], v[18:19], v[82:83]
	v_pk_fma_f32 v[74:75], v[74:75], v[30:31], v[94:95]
	v_pk_fma_f32 v[66:67], v[66:67], v[22:23], v[90:91]
	v_cndmask_b32_e64 v131, v132, v131, s[0:1]
	v_add_f32_e32 v98, v98, v99
	v_pk_add_f32 v[66:67], v[66:67], v[74:75]
	v_pk_add_f32 v[70:71], v[70:71], v[78:79]
	v_mul_f32_e32 v139, v160, v130
	v_mul_f32_e32 v98, v98, v131
	v_pk_add_f32 v[66:67], v[70:71], v[66:67]
	v_cmp_gt_u32_e32 vcc, 32, v1
	v_add_f32_e32 v66, v66, v67
	v_pk_mul_f32 v[92:93], v[92:93], v[40:41]
	v_cndmask_b32_e32 v67, v98, v139, vcc
	v_add_f32_e32 v67, s12, v67
	v_pk_mul_f32 v[96:97], v[96:97], v[48:49]
	v_pk_mul_f32 v[84:85], v[84:85], v[36:37]
	v_pk_mul_f32 v[88:89], v[88:89], v[44:45]
	v_mul_f32_e32 v67, 0xbfb8aa3b, v67
	v_pk_fma_f32 v[80:81], v[80:81], v[28:29], v[88:89]
	v_pk_fma_f32 v[72:73], v[72:73], v[20:21], v[84:85]
	v_pk_fma_f32 v[76:77], v[76:77], v[32:33], v[96:97]
	v_pk_fma_f32 v[68:69], v[68:69], v[24:25], v[92:93]
	v_exp_f32_e32 v70, v67
	v_pk_add_f32 v[68:69], v[68:69], v[76:77]
	v_pk_add_f32 v[72:73], v[72:73], v[80:81]
	v_cmp_lt_i32_e64 s[0:1], 0, v151
	v_pk_add_f32 v[68:69], v[72:73], v[68:69]
	v_mov_b32_e32 v137, v136
	v_add_f32_e32 v67, v68, v69
	v_add_f32_e32 v67, v66, v67
	v_add_f32_e32 v66, 1.0, v70
	v_rcp_f32_e32 v66, v66
	v_mov_b32_e32 v69, 0xff800000
	v_mov_b32_e32 v138, v133
	v_mov_b32_e32 v68, v67
	v_cndmask_b32_e64 v70, v69, v66, s[0:1]
	v_mbcnt_lo_u32_b32 v66, -1, 0
	v_mbcnt_hi_u32_b32 v66, -1, v66
	v_permlane32_swap_b32_e32 v136, v137
	v_permlane32_swap_b32_e32 v133, v138
	v_permlane32_swap_b32_e32 v67, v68
	v_and_b32_e32 v86, 64, v66
	s_mov_b32 s14, 8
	s_mov_b32 s13, 0
	v_mov_b32_e32 v66, 0
	s_waitcnt lgkmcnt(0)
